# baseline (speedup 1.0000x reference)
.LBB2_17:
	s_load_dword s42, s[0:1], 0x30
	s_load_dwordx8 s[8:15], s[0:1], 0x0
	v_lshrrev_b32_e32 v4, 5, v0
	v_and_b32_e32 v4, 4, v4
	v_lshrrev_b32_e32 v5, 3, v0
	v_lshrrev_b32_e32 v7, 1, v0
	v_lshlrev_b32_e32 v3, 4, v0
	s_movk_i32 s16, 0x70
	v_and_b32_e32 v6, 64, v1
	v_and_or_b32 v4, v5, 3, v4
	v_and_b32_e32 v7, 48, v7
	v_bitop3_b32 v2, v3, s16, v0 bitop3:0x48
	v_or3_b32 v6, v7, v6, v4
	s_waitcnt lgkmcnt(0)
	v_mad_u64_u32 v[146:147], s[16:17], s42, v5, v[2:3]
	v_mad_u64_u32 v[148:149], s[16:17], s42, v6, v[2:3]
	v_or_b32_e32 v3, 0x2000, v3
	v_lshrrev_b32_e32 v5, 7, v3
	v_lshrrev_b32_e32 v3, 6, v3
	v_and_b32_e32 v3, 0xc0, v3
	v_or3_b32 v3, v3, v7, v4
	v_mad_u64_u32 v[152:153], s[16:17], s42, v5, v[2:3]
	v_mad_u64_u32 v[154:155], s[16:17], s42, v3, v[2:3]
	s_ashr_i32 s43, s42, 31
	s_lshl_b64 s[36:37], s[42:43], 8
	s_ashr_i32 s16, s65, 31
	s_lshl_b32 s18, s42, 3
	s_mul_i32 s16, s36, s16
	s_mul_hi_u32 s17, s36, s65
	v_add_u32_e32 v150, s18, v148
	v_add_u32_e32 v156, s18, v154
	s_add_i32 s18, s17, s16
	s_lshr_b64 s[16:17], s[42:43], 24
	s_lshr_b32 s7, s19, 6
	s_mul_i32 s17, s16, s65
	s_lshr_b32 s40, s19, 8
	s_lshl_b64 s[34:35], s[42:43], 7
	s_lshl_b32 s66, s7, 10
	s_add_i32 s17, s18, s17
	v_writelane_b32 v189, s19, 0
	s_and_b64 s[18:19], s[4:5], exec
	s_cselect_b32 s18, s11, s15
	s_cselect_b32 s19, s10, s14
	s_ashr_i32 s21, s99, 31
	s_mul_i32 s21, s36, s21
	s_mul_hi_u32 s22, s36, s99
	s_add_i32 s21, s22, s21
	s_mul_i32 s16, s16, s99
	s_add_i32 s21, s21, s16
	s_mul_i32 s16, s36, s99
	s_add_u32 s56, s19, s16
	s_addc_u32 s57, s18, s21
	s_add_i32 s67, s66, 0
	s_add_i32 m0, s67, 0x10000
	s_mul_i32 s20, s36, s65
	global_load_lds_dwordx4 v148, s[56:57]
	s_add_i32 m0, s67, 0x12000
	s_and_b64 s[4:5], s[4:5], exec
	s_cselect_b32 s5, s8, s12
	s_cselect_b32 s4, s9, s13
	s_add_u32 s58, s5, s20
	global_load_lds_dwordx4 v154, s[56:57]
	s_addc_u32 s59, s4, s17
	s_mov_b32 m0, s67
	s_add_i32 s68, s67, 0x2000
	global_load_lds_dwordx4 v146, s[58:59]
	s_mov_b32 m0, s68
	v_mov_b32_e32 v149, 0
	global_load_lds_dwordx4 v152, s[58:59]
	s_add_i32 m0, s67, 0x14000
	v_mov_b32_e32 v155, v149
	global_load_lds_dwordx4 v150, s[56:57]
	s_add_i32 m0, s67, 0x16000
	s_add_u32 s4, s58, s34
	s_addc_u32 s5, s59, s35
	s_add_i32 s69, s67, 0x4000
	global_load_lds_dwordx4 v156, s[56:57]
	s_mov_b32 m0, s69
	s_add_i32 s70, s67, 0x6000
	global_load_lds_dwordx4 v146, s[4:5]
	s_mov_b32 m0, s70
	v_mov_b32_e32 v147, v149
	global_load_lds_dwordx4 v152, s[4:5]
	s_load_dwordx8 s[16:23], s[0:1], 0x38
	s_load_dwordx8 s[24:31], s[0:1], 0x58
	s_load_dword s38, s[0:1], 0x78
	s_load_dword s71, s[0:1], 0x138
	v_mov_b32_e32 v153, v149
	v_mov_b32_e32 v151, v149
	v_mov_b32_e32 v157, v149
	s_mov_b32 s72, 0
	v_lshl_add_u64 v[12:13], s[56:57], 0, v[148:149]
	v_lshl_add_u64 v[10:11], s[56:57], 0, v[154:155]
	v_lshl_add_u64 v[8:9], s[58:59], 0, v[146:147]
	v_lshl_add_u64 v[6:7], s[58:59], 0, v[152:153]
	v_lshl_add_u64 v[2:3], s[56:57], 0, v[150:151]
	s_cmp_lg_u32 s40, 1
	v_lshl_add_u64 v[4:5], s[56:57], 0, v[156:157]
	s_cbranch_scc1 .LBB2_19
	s_setprio 1
	s_barrier

.LBB2_41:
	ds_read_b128 v[2:5], v182
	ds_read_b128 v[10:13], v182 offset:2048
	ds_read_b128 v[6:9], v183
	ds_read_b128 v[14:17], v183 offset:2048
	s_add_i32 s62, s56, 2
	s_add_u32 s58, s4, 0x80
	s_addc_u32 s57, s5, 0
	s_cmp_eq_u32 s76, s56
	s_cselect_b32 s56, s52, s58
	s_cselect_b32 s57, s53, s57
	s_cselect_b32 s59, s55, s61
	s_cselect_b32 s58, s54, s60
	v_lshl_add_u64 v[166:167], s[4:5], 0, v[160:161]
	s_add_i32 m0, s67, 0xc000
	ds_read_b128 v[170:173], v184
	ds_read_b128 v[190:193], v184 offset:2048
	ds_read_b128 v[174:177], v185
	ds_read_b128 v[194:197], v185 offset:2048
	ds_read_b128 v[198:201], v184 offset:4096
	ds_read_b128 v[206:209], v184 offset:6144
	ds_read_b128 v[202:205], v185 offset:4096
	ds_read_b128 v[210:213], v185 offset:6144
	global_load_lds_dwordx4 v[166:167], off
	v_lshl_add_u64 v[166:167], s[4:5], 0, v[162:163]
	s_add_i32 m0, s67, 0xe000
	s_nop 0
	global_load_lds_dwordx4 v[166:167], off
	s_waitcnt lgkmcnt(8)
	s_barrier
	s_waitcnt lgkmcnt(0)
	s_waitcnt lgkmcnt(0)
	v_mfma_scale_f32_16x16x128_f8f6f4 v[142:145], v[2:9], v[170:177], v[142:145], v186, v186 op_sel_hi:[0,0,0]
	v_mfma_scale_f32_16x16x128_f8f6f4 v[138:141], v[10:17], v[170:177], v[138:141], v186, v186 op_sel_hi:[0,0,0]
	v_mfma_scale_f32_16x16x128_f8f6f4 v[126:129], v[2:9], v[190:197], v[126:129], v186, v186 op_sel_hi:[0,0,0]
	v_mfma_scale_f32_16x16x128_f8f6f4 v[122:125], v[10:17], v[190:197], v[122:125], v186, v186 op_sel_hi:[0,0,0]
	v_mfma_scale_f32_16x16x128_f8f6f4 v[110:113], v[2:9], v[198:205], v[110:113], v186, v186 op_sel_hi:[0,0,0]
	v_mfma_scale_f32_16x16x128_f8f6f4 v[106:109], v[10:17], v[198:205], v[106:109], v186, v186 op_sel_hi:[0,0,0]
	v_mfma_scale_f32_16x16x128_f8f6f4 v[94:97], v[2:9], v[206:213], v[94:97], v186, v186 op_sel_hi:[0,0,0]
	v_mfma_scale_f32_16x16x128_f8f6f4 v[90:93], v[10:17], v[206:213], v[90:93], v186, v186 op_sel_hi:[0,0,0]
	s_barrier
	s_add_i32 s63, s7, s66
	v_lshl_add_u64 v[166:167], s[58:59], 0, v[148:149]
	s_mov_b32 m0, s63
	ds_read_b128 v[214:217], v187
	ds_read_b128 v[222:225], v187 offset:2048
	ds_read_b128 v[218:221], v188
	ds_read_b128 v[226:229], v188 offset:2048
	global_load_lds_dwordx4 v[166:167], off
	v_lshl_add_u64 v[168:169], s[58:59], 0, v[154:155]
	s_add_i32 m0, s63, 0x2000
	s_nop 0
	global_load_lds_dwordx4 v[168:169], off
	s_barrier
	s_waitcnt lgkmcnt(0)
	s_waitcnt lgkmcnt(0)
	v_mfma_scale_f32_16x16x128_f8f6f4 v[134:137], v[214:221], v[170:177], v[134:137], v186, v186 op_sel_hi:[0,0,0]
	v_mfma_scale_f32_16x16x128_f8f6f4 v[130:133], v[222:229], v[170:177], v[130:133], v186, v186 op_sel_hi:[0,0,0]
	v_mfma_scale_f32_16x16x128_f8f6f4 v[118:121], v[214:221], v[190:197], v[118:121], v186, v186 op_sel_hi:[0,0,0]
	v_mfma_scale_f32_16x16x128_f8f6f4 v[114:117], v[222:229], v[190:197], v[114:117], v186, v186 op_sel_hi:[0,0,0]
	v_mfma_scale_f32_16x16x128_f8f6f4 v[102:105], v[214:221], v[198:205], v[102:105], v186, v186 op_sel_hi:[0,0,0]
	v_mfma_scale_f32_16x16x128_f8f6f4 v[98:101], v[222:229], v[198:205], v[98:101], v186, v186 op_sel_hi:[0,0,0]
	v_mfma_scale_f32_16x16x128_f8f6f4 v[86:89], v[214:221], v[206:213], v[86:89], v186, v186 op_sel_hi:[0,0,0]
	v_mfma_scale_f32_16x16x128_f8f6f4 v[82:85], v[222:229], v[206:213], v[82:85], v186, v186 op_sel_hi:[0,0,0]
	s_mov_b32 m0, s67
	v_lshl_add_u64 v[170:171], s[56:57], 0, v[146:147]
	s_barrier
	ds_read_b128 v[190:193], v184 offset:16384
	ds_read_b128 v[198:201], v184 offset:18432
	ds_read_b128 v[194:197], v185 offset:16384
	ds_read_b128 v[202:205], v185 offset:18432
	ds_read_b128 v[206:209], v184 offset:20480
	ds_read_b128 v[230:233], v184 offset:22528
	ds_read_b128 v[210:213], v185 offset:20480
	ds_read_b128 v[234:237], v185 offset:22528
	global_load_lds_dwordx4 v[170:171], off
	v_lshl_add_u64 v[172:173], s[56:57], 0, v[152:153]
	s_mov_b32 m0, s68
	s_nop 0
	global_load_lds_dwordx4 v[172:173], off
	s_barrier
	s_waitcnt lgkmcnt(0)
	s_waitcnt lgkmcnt(0)
	v_mfma_scale_f32_16x16x128_f8f6f4 v[78:81], v[2:9], v[190:197], v[78:81], v186, v186 op_sel_hi:[0,0,0]
	v_mfma_scale_f32_16x16x128_f8f6f4 v[74:77], v[10:17], v[190:197], v[74:77], v186, v186 op_sel_hi:[0,0,0]
	v_mfma_scale_f32_16x16x128_f8f6f4 v[62:65], v[2:9], v[198:205], v[62:65], v186, v186 op_sel_hi:[0,0,0]
	v_mfma_scale_f32_16x16x128_f8f6f4 v[58:61], v[10:17], v[198:205], v[58:61], v186, v186 op_sel_hi:[0,0,0]
	v_mfma_scale_f32_16x16x128_f8f6f4 v[46:49], v[2:9], v[206:213], v[46:49], v186, v186 op_sel_hi:[0,0,0]
	v_mfma_scale_f32_16x16x128_f8f6f4 v[42:45], v[10:17], v[206:213], v[42:45], v186, v186 op_sel_hi:[0,0,0]
	v_mfma_scale_f32_16x16x128_f8f6f4 v[30:33], v[2:9], v[230:237], v[30:33], v186, v186 op_sel_hi:[0,0,0]
	v_mfma_scale_f32_16x16x128_f8f6f4 v[26:29], v[10:17], v[230:237], v[26:29], v186, v186 op_sel_hi:[0,0,0]
	s_barrier
	s_add_i32 s63, s95, s66
	v_lshl_add_u64 v[2:3], s[58:59], 0, v[150:151]
	s_mov_b32 m0, s63
	v_lshl_add_u64 v[4:5], s[58:59], 0, v[156:157]
	global_load_lds_dwordx4 v[2:3], off
	s_add_i32 m0, s63, 0x2000
	s_nop 0
	global_load_lds_dwordx4 v[4:5], off
	s_waitcnt vmcnt(6)
	s_barrier
	v_mfma_scale_f32_16x16x128_f8f6f4 v[70:73], v[214:221], v[190:197], v[70:73], v186, v186 op_sel_hi:[0,0,0]
	v_mfma_scale_f32_16x16x128_f8f6f4 v[66:69], v[222:229], v[190:197], v[66:69], v186, v186 op_sel_hi:[0,0,0]
	v_mfma_scale_f32_16x16x128_f8f6f4 v[54:57], v[214:221], v[198:205], v[54:57], v186, v186 op_sel_hi:[0,0,0]
	v_mfma_scale_f32_16x16x128_f8f6f4 v[50:53], v[222:229], v[198:205], v[50:53], v186, v186 op_sel_hi:[0,0,0]
	v_mfma_scale_f32_16x16x128_f8f6f4 v[38:41], v[214:221], v[206:213], v[38:41], v186, v186 op_sel_hi:[0,0,0]
	v_mfma_scale_f32_16x16x128_f8f6f4 v[34:37], v[222:229], v[206:213], v[34:37], v186, v186 op_sel_hi:[0,0,0]
	v_mfma_scale_f32_16x16x128_f8f6f4 v[22:25], v[214:221], v[230:237], v[22:25], v186, v186 op_sel_hi:[0,0,0]
	v_mfma_scale_f32_16x16x128_f8f6f4 v[18:21], v[222:229], v[230:237], v[18:21], v186, v186 op_sel_hi:[0,0,0]
	s_add_i32 s58, 0, 0x18000
	v_add_u32_e32 v10, s58, v179
	s_barrier
	v_add_u32_e32 v14, s58, v180
	ds_read_b128 v[6:9], v10
	ds_read_b128 v[190:193], v10 offset:2048
	ds_read_b128 v[10:13], v14
	ds_read_b128 v[194:197], v14 offset:2048
	s_add_u32 s56, s56, s34
	s_addc_u32 s57, s57, s35
	s_mov_b32 m0, s69
	v_lshl_add_u64 v[14:15], s[56:57], 0, v[146:147]
	ds_read_b128 v[198:201], v184 offset:32768
	ds_read_b128 v[206:209], v184 offset:34816
	ds_read_b128 v[202:205], v185 offset:32768
	ds_read_b128 v[210:213], v185 offset:34816
	ds_read_b128 v[214:217], v184 offset:36864
	ds_read_b128 v[222:225], v184 offset:38912
	ds_read_b128 v[218:221], v185 offset:36864
	ds_read_b128 v[226:229], v185 offset:38912
	global_load_lds_dwordx4 v[14:15], off
	v_lshl_add_u64 v[14:15], s[56:57], 0, v[152:153]
	s_mov_b32 m0, s70
	s_nop 0
	global_load_lds_dwordx4 v[14:15], off
	s_waitcnt lgkmcnt(8)
	s_barrier
	s_waitcnt lgkmcnt(0)
	s_waitcnt lgkmcnt(0)
	v_mfma_scale_f32_16x16x128_f8f6f4 v[142:145], v[6:13], v[198:205], v[142:145], v186, v186 op_sel_hi:[0,0,0]
	v_mfma_scale_f32_16x16x128_f8f6f4 v[138:141], v[190:197], v[198:205], v[138:141], v186, v186 op_sel_hi:[0,0,0]
	v_mfma_scale_f32_16x16x128_f8f6f4 v[126:129], v[6:13], v[206:213], v[126:129], v186, v186 op_sel_hi:[0,0,0]
	v_mfma_scale_f32_16x16x128_f8f6f4 v[122:125], v[190:197], v[206:213], v[122:125], v186, v186 op_sel_hi:[0,0,0]
	v_mfma_scale_f32_16x16x128_f8f6f4 v[110:113], v[6:13], v[214:221], v[110:113], v186, v186 op_sel_hi:[0,0,0]
	v_mfma_scale_f32_16x16x128_f8f6f4 v[106:109], v[190:197], v[214:221], v[106:109], v186, v186 op_sel_hi:[0,0,0]
	v_mfma_scale_f32_16x16x128_f8f6f4 v[94:97], v[6:13], v[222:229], v[94:97], v186, v186 op_sel_hi:[0,0,0]
	v_mfma_scale_f32_16x16x128_f8f6f4 v[90:93], v[190:197], v[222:229], v[90:93], v186, v186 op_sel_hi:[0,0,0]
	s_barrier
	s_add_i32 s56, 0, 0x1c000
	v_add_u32_e32 v14, s56, v179
	v_add_u32_e32 v15, s56, v180
	s_add_i32 s57, s58, s66
	ds_read_b128 v[230:233], v14
	ds_read_b128 v[238:241], v14 offset:2048
	ds_read_b128 v[234:237], v15
	ds_read_b128 v[242:245], v15 offset:2048
	v_lshl_add_u64 v[14:15], v[166:167], 0, s[40:41]
	s_mov_b32 m0, s57
	s_nop 0
	global_load_lds_dwordx4 v[14:15], off
	v_lshl_add_u64 v[14:15], v[168:169], 0, s[40:41]
	s_add_i32 m0, s57, 0x2000
	s_nop 0
	global_load_lds_dwordx4 v[14:15], off
	s_barrier
	s_waitcnt lgkmcnt(0)
	s_waitcnt lgkmcnt(0)
	v_mfma_scale_f32_16x16x128_f8f6f4 v[134:137], v[230:237], v[198:205], v[134:137], v186, v186 op_sel_hi:[0,0,0]
	v_mfma_scale_f32_16x16x128_f8f6f4 v[130:133], v[238:245], v[198:205], v[130:133], v186, v186 op_sel_hi:[0,0,0]
	v_mfma_scale_f32_16x16x128_f8f6f4 v[118:121], v[230:237], v[206:213], v[118:121], v186, v186 op_sel_hi:[0,0,0]
	v_mfma_scale_f32_16x16x128_f8f6f4 v[114:117], v[238:245], v[206:213], v[114:117], v186, v186 op_sel_hi:[0,0,0]
	v_mfma_scale_f32_16x16x128_f8f6f4 v[102:105], v[230:237], v[214:221], v[102:105], v186, v186 op_sel_hi:[0,0,0]
	v_mfma_scale_f32_16x16x128_f8f6f4 v[98:101], v[238:245], v[214:221], v[98:101], v186, v186 op_sel_hi:[0,0,0]
	v_mfma_scale_f32_16x16x128_f8f6f4 v[86:89], v[230:237], v[222:229], v[86:89], v186, v186 op_sel_hi:[0,0,0]
	v_mfma_scale_f32_16x16x128_f8f6f4 v[82:85], v[238:245], v[222:229], v[82:85], v186, v186 op_sel_hi:[0,0,0]
	s_mov_b32 m0, s74
	v_lshl_add_u64 v[14:15], v[170:171], 0, s[40:41]
	s_barrier
	ds_read_b128 v[198:201], v184 offset:49152
	ds_read_b128 v[206:209], v184 offset:51200
	ds_read_b128 v[202:205], v185 offset:49152
	ds_read_b128 v[210:213], v185 offset:51200
	ds_read_b128 v[214:217], v184 offset:53248
	ds_read_b128 v[222:225], v184 offset:55296
	ds_read_b128 v[218:221], v185 offset:53248
	ds_read_b128 v[226:229], v185 offset:55296
	global_load_lds_dwordx4 v[14:15], off
	v_lshl_add_u64 v[14:15], v[172:173], 0, s[40:41]
	s_mov_b32 m0, s75
	s_nop 0
	global_load_lds_dwordx4 v[14:15], off
	s_barrier
	s_waitcnt lgkmcnt(0)
	s_waitcnt lgkmcnt(0)
	v_mfma_scale_f32_16x16x128_f8f6f4 v[78:81], v[6:13], v[198:205], v[78:81], v186, v186 op_sel_hi:[0,0,0]
	v_mfma_scale_f32_16x16x128_f8f6f4 v[74:77], v[190:197], v[198:205], v[74:77], v186, v186 op_sel_hi:[0,0,0]
	v_mfma_scale_f32_16x16x128_f8f6f4 v[62:65], v[6:13], v[206:213], v[62:65], v186, v186 op_sel_hi:[0,0,0]
	v_mfma_scale_f32_16x16x128_f8f6f4 v[58:61], v[190:197], v[206:213], v[58:61], v186, v186 op_sel_hi:[0,0,0]
	v_mfma_scale_f32_16x16x128_f8f6f4 v[46:49], v[6:13], v[214:221], v[46:49], v186, v186 op_sel_hi:[0,0,0]
	v_mfma_scale_f32_16x16x128_f8f6f4 v[42:45], v[190:197], v[214:221], v[42:45], v186, v186 op_sel_hi:[0,0,0]
	v_mfma_scale_f32_16x16x128_f8f6f4 v[30:33], v[6:13], v[222:229], v[30:33], v186, v186 op_sel_hi:[0,0,0]
	v_mfma_scale_f32_16x16x128_f8f6f4 v[26:29], v[190:197], v[222:229], v[26:29], v186, v186 op_sel_hi:[0,0,0]
	s_barrier
	s_add_i32 s56, s56, s66
	v_lshl_add_u64 v[2:3], v[2:3], 0, s[40:41]
	s_mov_b32 m0, s56
	s_nop 0
	global_load_lds_dwordx4 v[2:3], off
	v_lshl_add_u64 v[2:3], v[4:5], 0, s[40:41]
	s_add_i32 m0, s56, 0x2000
	s_nop 0
	global_load_lds_dwordx4 v[2:3], off
	s_waitcnt vmcnt(6)
	s_barrier
	v_mfma_scale_f32_16x16x128_f8f6f4 v[70:73], v[230:237], v[198:205], v[70:73], v186, v186 op_sel_hi:[0,0,0]
	v_mfma_scale_f32_16x16x128_f8f6f4 v[66:69], v[238:245], v[198:205], v[66:69], v186, v186 op_sel_hi:[0,0,0]
	v_mfma_scale_f32_16x16x128_f8f6f4 v[54:57], v[230:237], v[206:213], v[54:57], v186, v186 op_sel_hi:[0,0,0]
	v_mfma_scale_f32_16x16x128_f8f6f4 v[50:53], v[238:245], v[206:213], v[50:53], v186, v186 op_sel_hi:[0,0,0]
	v_mfma_scale_f32_16x16x128_f8f6f4 v[38:41], v[230:237], v[214:221], v[38:41], v186, v186 op_sel_hi:[0,0,0]
	v_mfma_scale_f32_16x16x128_f8f6f4 v[34:37], v[238:245], v[214:221], v[34:37], v186, v186 op_sel_hi:[0,0,0]
	v_mfma_scale_f32_16x16x128_f8f6f4 v[22:25], v[230:237], v[222:229], v[22:25], v186, v186 op_sel_hi:[0,0,0]
	v_mfma_scale_f32_16x16x128_f8f6f4 v[18:21], v[238:245], v[222:229], v[18:21], v186, v186 op_sel_hi:[0,0,0]
	s_add_u32 s4, s4, 0x100
	s_addc_u32 s5, s5, 0
	s_add_u32 s60, s60, 0x100
	s_addc_u32 s61, s61, 0
	s_cmp_ge_i32 s62, s73
	s_mov_b32 s56, s62
	s_barrier
	s_cbranch_scc0 .LBB2_41

.LBB7_7:
	s_load_dword s38, s[0:1], 0x30
	v_lshrrev_b32_e32 v4, 5, v0
	v_lshlrev_b32_e32 v3, 4, v0
	v_and_b32_e32 v4, 4, v4
	v_lshrrev_b32_e32 v5, 3, v0
	v_xor_b32_e32 v2, v3, v0
	v_and_or_b32 v7, v5, 3, v4
	v_lshrrev_b32_e32 v4, 1, v0
	v_lshrrev_b32_e32 v2, 1, v2
	v_and_b32_e32 v6, 64, v1
	v_and_b32_e32 v8, 48, v4
	v_and_b32_e32 v2, 56, v2
	v_or3_b32 v4, v8, v6, v7
	s_waitcnt lgkmcnt(0)
	v_mul_lo_u32 v5, s38, v5
	v_add_lshl_u32 v146, v5, v2, 1
	v_mad_u64_u32 v[4:5], s[22:23], s38, v4, v[2:3]
	s_lshl_b32 s24, s38, 3
	v_or_b32_e32 v3, 0x2000, v3
	v_lshlrev_b32_e32 v148, 1, v4
	v_add_lshl_u32 v150, v4, s24, 1
	v_lshrrev_b32_e32 v4, 7, v3
	v_lshrrev_b32_e32 v3, 6, v3
	v_and_b32_e32 v3, 0xc0, v3
	v_or3_b32 v3, v3, v8, v7
	v_mul_lo_u32 v4, s38, v4
	v_add_lshl_u32 v152, v4, v2, 1
	v_mad_u64_u32 v[2:3], s[22:23], s38, v3, v[2:3]
	s_ashr_i32 s39, s38, 31
	s_lshl_b64 s[30:31], s[38:39], 9
	s_ashr_i32 s22, s72, 31
	s_mul_i32 s22, s30, s22
	s_mul_hi_u32 s23, s30, s72
	s_ashr_i32 s25, s73, 31
	v_add_lshl_u32 v156, v2, s24, 1
	s_add_i32 s24, s23, s22
	s_lshr_b64 s[22:23], s[38:39], 23
	s_mul_i32 s25, s30, s25
	s_mul_hi_u32 s26, s30, s73
	s_lshr_b32 s7, s19, 6
	s_mul_i32 s23, s22, s72
	s_add_i32 s25, s26, s25
	s_mul_i32 s22, s22, s73
	s_lshr_b32 s41, s19, 8
	s_lshl_b64 s[28:29], s[38:39], 8
	s_lshl_b32 s54, s7, 10
	s_add_i32 s24, s24, s23
	s_add_i32 s25, s25, s22
	s_mul_i32 s22, s30, s73
	s_add_u32 s50, s20, s22
	s_addc_u32 s51, s21, s25
	s_add_i32 s55, s54, 0
	s_add_i32 m0, s55, 0x10000
	s_mul_i32 s23, s30, s72
	global_load_lds_dwordx4 v148, s[50:51]
	s_add_i32 m0, s55, 0x12000
	v_lshlrev_b32_e32 v154, 1, v2
	s_add_u32 s4, s4, s23
	global_load_lds_dwordx4 v154, s[50:51]
	s_addc_u32 s5, s5, s24
	s_mov_b32 m0, s55
	s_add_i32 s56, s55, 0x2000
	global_load_lds_dwordx4 v146, s[4:5]
	s_mov_b32 m0, s56
	v_mov_b32_e32 v149, 0
	global_load_lds_dwordx4 v152, s[4:5]
	s_add_i32 m0, s55, 0x14000
	v_mov_b32_e32 v155, v149
	global_load_lds_dwordx4 v150, s[50:51]
	s_add_i32 m0, s55, 0x16000
	s_add_u32 s20, s4, s28
	s_addc_u32 s21, s5, s29
	s_add_i32 s57, s55, 0x4000
	global_load_lds_dwordx4 v156, s[50:51]
	s_mov_b32 m0, s57
	s_add_i32 s58, s55, 0x6000
	global_load_lds_dwordx4 v146, s[20:21]
	s_mov_b32 m0, s58
	v_mov_b32_e32 v147, v149
	global_load_lds_dwordx4 v152, s[20:21]
	s_load_dwordx4 s[20:23], s[0:1], 0x38
	s_load_dwordx2 s[34:35], s[0:1], 0x48
	s_load_dwordx4 s[24:27], s[0:1], 0x68
	s_load_dword s59, s[0:1], 0x78
	s_load_dword s60, s[0:1], 0x138
	v_mov_b32_e32 v153, v149
	v_mov_b32_e32 v151, v149
	v_mov_b32_e32 v157, v149
	s_mov_b32 s61, 0
	v_lshl_add_u64 v[12:13], s[50:51], 0, v[148:149]
	v_lshl_add_u64 v[10:11], s[50:51], 0, v[154:155]
	v_lshl_add_u64 v[8:9], s[4:5], 0, v[146:147]
	v_lshl_add_u64 v[6:7], s[4:5], 0, v[152:153]
	v_lshl_add_u64 v[2:3], s[50:51], 0, v[150:151]
	s_cmp_lg_u32 s41, 1
	v_lshl_add_u64 v[4:5], s[50:51], 0, v[156:157]
	s_cbranch_scc1 .LBB7_9
	s_setprio 1
	s_barrier

.LBB7_21:
	ds_read_b128 v[130:133], v172
	ds_read_b128 v[134:137], v173
	ds_read_b128 v[138:141], v174
	ds_read_b128 v[142:145], v175
	s_add_i32 s77, s50, 2
	s_add_u32 s52, s4, 0x80
	s_addc_u32 s51, s5, 0
	s_cmp_eq_u32 s65, s50
	s_cselect_b32 s50, s46, s52
	s_cselect_b32 s51, s47, s51
	s_cselect_b32 s53, s49, s76
	s_cselect_b32 s52, s48, s75
	v_lshl_add_u64 v[214:215], s[4:5], 0, v[158:159]
	s_add_i32 m0, s55, 0xc000
	ds_read_b128 v[164:167], v176
	ds_read_b128 v[186:189], v176 offset:2048
	ds_read_b128 v[190:193], v177
	ds_read_b128 v[194:197], v177 offset:2048
	ds_read_b128 v[198:201], v176 offset:4096
	ds_read_b128 v[202:205], v176 offset:6144
	ds_read_b128 v[206:209], v177 offset:4096
	ds_read_b128 v[210:213], v177 offset:6144
	global_load_lds_dwordx4 v[214:215], off
	v_lshl_add_u64 v[214:215], s[4:5], 0, v[160:161]
	s_add_i32 m0, s55, 0xe000
	s_nop 0
	global_load_lds_dwordx4 v[214:215], off
	s_waitcnt lgkmcnt(8)
	s_barrier
	s_waitcnt lgkmcnt(0)
	s_waitcnt lgkmcnt(0)
	v_mfma_f32_16x16x32_f16 v[126:129], v[130:133], v[164:167], v[126:129]
	v_mfma_f32_16x16x32_f16 v[122:125], v[138:141], v[164:167], v[122:125]
	v_mfma_f32_16x16x32_f16 v[110:113], v[130:133], v[186:189], v[110:113]
	v_mfma_f32_16x16x32_f16 v[106:109], v[138:141], v[186:189], v[106:109]
	v_mfma_f32_16x16x32_f16 v[94:97], v[130:133], v[198:201], v[94:97]
	v_mfma_f32_16x16x32_f16 v[90:93], v[138:141], v[198:201], v[90:93]
	v_mfma_f32_16x16x32_f16 v[78:81], v[130:133], v[202:205], v[78:81]
	v_mfma_f32_16x16x32_f16 v[74:77], v[138:141], v[202:205], v[74:77]
	v_mfma_f32_16x16x32_f16 v[126:129], v[134:137], v[190:193], v[126:129]
	v_mfma_f32_16x16x32_f16 v[122:125], v[142:145], v[190:193], v[122:125]
	v_mfma_f32_16x16x32_f16 v[110:113], v[134:137], v[194:197], v[110:113]
	v_mfma_f32_16x16x32_f16 v[106:109], v[142:145], v[194:197], v[106:109]
	v_mfma_f32_16x16x32_f16 v[94:97], v[134:137], v[206:209], v[94:97]
	v_mfma_f32_16x16x32_f16 v[90:93], v[142:145], v[206:209], v[90:93]
	v_mfma_f32_16x16x32_f16 v[78:81], v[134:137], v[210:213], v[78:81]
	v_mfma_f32_16x16x32_f16 v[74:77], v[142:145], v[210:213], v[74:77]
	s_barrier
	s_add_i32 s78, s7, s54
	v_lshl_add_u64 v[230:231], s[52:53], 0, v[148:149]
	s_mov_b32 m0, s78
	ds_read_b128 v[214:217], v178
	ds_read_b128 v[218:221], v179
	ds_read_b128 v[222:225], v180
	ds_read_b128 v[226:229], v181
	global_load_lds_dwordx4 v[230:231], off
	v_lshl_add_u64 v[232:233], s[52:53], 0, v[154:155]
	s_add_i32 m0, s78, 0x2000
	s_nop 0
	global_load_lds_dwordx4 v[232:233], off
	s_barrier
	s_waitcnt lgkmcnt(0)
	s_waitcnt lgkmcnt(0)
	v_mfma_f32_16x16x32_f16 v[118:121], v[214:217], v[164:167], v[118:121]
	v_mfma_f32_16x16x32_f16 v[114:117], v[222:225], v[164:167], v[114:117]
	v_mfma_f32_16x16x32_f16 v[102:105], v[214:217], v[186:189], v[102:105]
	v_mfma_f32_16x16x32_f16 v[98:101], v[222:225], v[186:189], v[98:101]
	v_mfma_f32_16x16x32_f16 v[86:89], v[214:217], v[198:201], v[86:89]
	v_mfma_f32_16x16x32_f16 v[82:85], v[222:225], v[198:201], v[82:85]
	v_mfma_f32_16x16x32_f16 v[70:73], v[214:217], v[202:205], v[70:73]
	v_mfma_f32_16x16x32_f16 v[66:69], v[222:225], v[202:205], v[66:69]
	v_mfma_f32_16x16x32_f16 v[118:121], v[218:221], v[190:193], v[118:121]
	v_mfma_f32_16x16x32_f16 v[114:117], v[226:229], v[190:193], v[114:117]
	v_mfma_f32_16x16x32_f16 v[102:105], v[218:221], v[194:197], v[102:105]
	v_mfma_f32_16x16x32_f16 v[98:101], v[226:229], v[194:197], v[98:101]
	v_mfma_f32_16x16x32_f16 v[86:89], v[218:221], v[206:209], v[86:89]
	v_mfma_f32_16x16x32_f16 v[82:85], v[226:229], v[206:209], v[82:85]
	v_mfma_f32_16x16x32_f16 v[70:73], v[218:221], v[210:213], v[70:73]
	v_mfma_f32_16x16x32_f16 v[66:69], v[226:229], v[210:213], v[66:69]
	s_mov_b32 m0, s55
	v_lshl_add_u64 v[234:235], s[50:51], 0, v[146:147]
	s_barrier
	ds_read_b128 v[164:167], v176 offset:16384
	ds_read_b128 v[186:189], v176 offset:18432
	ds_read_b128 v[190:193], v177 offset:16384
	ds_read_b128 v[194:197], v177 offset:18432
	ds_read_b128 v[198:201], v176 offset:20480
	ds_read_b128 v[202:205], v176 offset:22528
	ds_read_b128 v[206:209], v177 offset:20480
	ds_read_b128 v[210:213], v177 offset:22528
	global_load_lds_dwordx4 v[234:235], off
	v_lshl_add_u64 v[236:237], s[50:51], 0, v[152:153]
	s_mov_b32 m0, s56
	s_nop 0
	global_load_lds_dwordx4 v[236:237], off
	s_barrier
	s_waitcnt lgkmcnt(0)
	s_waitcnt lgkmcnt(0)
	v_mfma_f32_16x16x32_f16 v[62:65], v[130:133], v[164:167], v[62:65]
	v_mfma_f32_16x16x32_f16 v[58:61], v[138:141], v[164:167], v[58:61]
	v_mfma_f32_16x16x32_f16 v[46:49], v[130:133], v[186:189], v[46:49]
	v_mfma_f32_16x16x32_f16 v[42:45], v[138:141], v[186:189], v[42:45]
	v_mfma_f32_16x16x32_f16 v[30:33], v[130:133], v[198:201], v[30:33]
	v_mfma_f32_16x16x32_f16 v[26:29], v[138:141], v[198:201], v[26:29]
	v_mfma_f32_16x16x32_f16 v[14:17], v[130:133], v[202:205], v[14:17]
	v_mfma_f32_16x16x32_f16 v[10:13], v[138:141], v[202:205], v[10:13]
	v_mfma_f32_16x16x32_f16 v[62:65], v[134:137], v[190:193], v[62:65]
	v_mfma_f32_16x16x32_f16 v[58:61], v[142:145], v[190:193], v[58:61]
	v_mfma_f32_16x16x32_f16 v[46:49], v[134:137], v[194:197], v[46:49]
	v_mfma_f32_16x16x32_f16 v[42:45], v[142:145], v[194:197], v[42:45]
	v_mfma_f32_16x16x32_f16 v[30:33], v[134:137], v[206:209], v[30:33]
	v_mfma_f32_16x16x32_f16 v[26:29], v[142:145], v[206:209], v[26:29]
	v_mfma_f32_16x16x32_f16 v[14:17], v[134:137], v[210:213], v[14:17]
	v_mfma_f32_16x16x32_f16 v[10:13], v[142:145], v[210:213], v[10:13]
	s_barrier
	s_add_i32 s78, s68, s54
	v_lshl_add_u64 v[238:239], s[52:53], 0, v[150:151]
	s_mov_b32 m0, s78
	v_lshl_add_u64 v[240:241], s[52:53], 0, v[156:157]
	global_load_lds_dwordx4 v[238:239], off
	s_add_i32 m0, s78, 0x2000
	s_nop 0
	global_load_lds_dwordx4 v[240:241], off
	s_waitcnt vmcnt(6)
	s_barrier
	v_mfma_f32_16x16x32_f16 v[54:57], v[214:217], v[164:167], v[54:57]
	v_mfma_f32_16x16x32_f16 v[50:53], v[222:225], v[164:167], v[50:53]
	v_mfma_f32_16x16x32_f16 v[38:41], v[214:217], v[186:189], v[38:41]
	v_mfma_f32_16x16x32_f16 v[34:37], v[222:225], v[186:189], v[34:37]
	v_mfma_f32_16x16x32_f16 v[22:25], v[214:217], v[198:201], v[22:25]
	v_mfma_f32_16x16x32_f16 v[18:21], v[222:225], v[198:201], v[18:21]
	v_mfma_f32_16x16x32_f16 v[6:9], v[214:217], v[202:205], v[6:9]
	v_mfma_f32_16x16x32_f16 v[2:5], v[222:225], v[202:205], v[2:5]
	v_mfma_f32_16x16x32_f16 v[54:57], v[218:221], v[190:193], v[54:57]
	v_mfma_f32_16x16x32_f16 v[50:53], v[226:229], v[190:193], v[50:53]
	v_mfma_f32_16x16x32_f16 v[38:41], v[218:221], v[194:197], v[38:41]
	v_mfma_f32_16x16x32_f16 v[34:37], v[226:229], v[194:197], v[34:37]
	v_mfma_f32_16x16x32_f16 v[22:25], v[218:221], v[206:209], v[22:25]
	v_mfma_f32_16x16x32_f16 v[18:21], v[226:229], v[206:209], v[18:21]
	v_mfma_f32_16x16x32_f16 v[6:9], v[218:221], v[210:213], v[6:9]
	v_mfma_f32_16x16x32_f16 v[2:5], v[226:229], v[210:213], v[2:5]
	s_add_i32 s52, 0, 0x18000
	v_add_u32_e32 v130, s52, v169
	v_add_u32_e32 v134, s52, v170
	s_barrier
	ds_read_b128 v[130:133], v130
	ds_read_b128 v[134:137], v134
	ds_read_b128 v[138:141], v182
	ds_read_b128 v[142:145], v183
	s_add_u32 s50, s50, s28
	s_addc_u32 s51, s51, s29
	s_mov_b32 m0, s57
	v_lshl_add_u64 v[214:215], s[50:51], 0, v[146:147]
	ds_read_b128 v[164:167], v176 offset:32768
	ds_read_b128 v[186:189], v176 offset:34816
	ds_read_b128 v[190:193], v177 offset:32768
	ds_read_b128 v[194:197], v177 offset:34816
	ds_read_b128 v[198:201], v176 offset:36864
	ds_read_b128 v[202:205], v176 offset:38912
	ds_read_b128 v[206:209], v177 offset:36864
	ds_read_b128 v[210:213], v177 offset:38912
	global_load_lds_dwordx4 v[214:215], off
	v_lshl_add_u64 v[214:215], s[50:51], 0, v[152:153]
	s_mov_b32 m0, s58
	s_nop 0
	global_load_lds_dwordx4 v[214:215], off
	s_waitcnt lgkmcnt(8)
	s_barrier
	s_waitcnt lgkmcnt(0)
	s_waitcnt lgkmcnt(0)
	v_mfma_f32_16x16x32_f16 v[126:129], v[130:133], v[164:167], v[126:129]
	v_mfma_f32_16x16x32_f16 v[122:125], v[138:141], v[164:167], v[122:125]
	v_mfma_f32_16x16x32_f16 v[110:113], v[130:133], v[186:189], v[110:113]
	v_mfma_f32_16x16x32_f16 v[106:109], v[138:141], v[186:189], v[106:109]
	v_mfma_f32_16x16x32_f16 v[94:97], v[130:133], v[198:201], v[94:97]
	v_mfma_f32_16x16x32_f16 v[90:93], v[138:141], v[198:201], v[90:93]
	v_mfma_f32_16x16x32_f16 v[78:81], v[130:133], v[202:205], v[78:81]
	v_mfma_f32_16x16x32_f16 v[74:77], v[138:141], v[202:205], v[74:77]
	v_mfma_f32_16x16x32_f16 v[126:129], v[134:137], v[190:193], v[126:129]
	v_mfma_f32_16x16x32_f16 v[122:125], v[142:145], v[190:193], v[122:125]
	v_mfma_f32_16x16x32_f16 v[110:113], v[134:137], v[194:197], v[110:113]
	v_mfma_f32_16x16x32_f16 v[106:109], v[142:145], v[194:197], v[106:109]
	v_mfma_f32_16x16x32_f16 v[94:97], v[134:137], v[206:209], v[94:97]
	v_mfma_f32_16x16x32_f16 v[90:93], v[142:145], v[206:209], v[90:93]
	v_mfma_f32_16x16x32_f16 v[78:81], v[134:137], v[210:213], v[78:81]
	v_mfma_f32_16x16x32_f16 v[74:77], v[142:145], v[210:213], v[74:77]
	s_barrier
	s_add_i32 s50, 0, 0x1c000
	s_add_i32 s51, s52, s54
	v_add_u32_e32 v214, s50, v169
	v_add_u32_e32 v218, s50, v170
	v_lshl_add_u64 v[230:231], v[230:231], 0, s[36:37]
	s_mov_b32 m0, s51
	ds_read_b128 v[214:217], v214
	ds_read_b128 v[218:221], v218
	ds_read_b128 v[222:225], v184
	ds_read_b128 v[226:229], v185
	global_load_lds_dwordx4 v[230:231], off
	v_lshl_add_u64 v[230:231], v[232:233], 0, s[36:37]
	s_add_i32 m0, s51, 0x2000
	s_nop 0
	global_load_lds_dwordx4 v[230:231], off
	s_barrier
	s_waitcnt lgkmcnt(0)
	s_waitcnt lgkmcnt(0)
	v_mfma_f32_16x16x32_f16 v[118:121], v[214:217], v[164:167], v[118:121]
	v_mfma_f32_16x16x32_f16 v[114:117], v[222:225], v[164:167], v[114:117]
	v_mfma_f32_16x16x32_f16 v[102:105], v[214:217], v[186:189], v[102:105]
	v_mfma_f32_16x16x32_f16 v[98:101], v[222:225], v[186:189], v[98:101]
	v_mfma_f32_16x16x32_f16 v[86:89], v[214:217], v[198:201], v[86:89]
	v_mfma_f32_16x16x32_f16 v[82:85], v[222:225], v[198:201], v[82:85]
	v_mfma_f32_16x16x32_f16 v[70:73], v[214:217], v[202:205], v[70:73]
	v_mfma_f32_16x16x32_f16 v[66:69], v[222:225], v[202:205], v[66:69]
	v_mfma_f32_16x16x32_f16 v[118:121], v[218:221], v[190:193], v[118:121]
	v_mfma_f32_16x16x32_f16 v[114:117], v[226:229], v[190:193], v[114:117]
	v_mfma_f32_16x16x32_f16 v[102:105], v[218:221], v[194:197], v[102:105]
	v_mfma_f32_16x16x32_f16 v[98:101], v[226:229], v[194:197], v[98:101]
	v_mfma_f32_16x16x32_f16 v[86:89], v[218:221], v[206:209], v[86:89]
	v_mfma_f32_16x16x32_f16 v[82:85], v[226:229], v[206:209], v[82:85]
	v_mfma_f32_16x16x32_f16 v[70:73], v[218:221], v[210:213], v[70:73]
	v_mfma_f32_16x16x32_f16 v[66:69], v[226:229], v[210:213], v[66:69]
	s_mov_b32 m0, s62
	v_lshl_add_u64 v[230:231], v[234:235], 0, s[36:37]
	s_barrier
	ds_read_b128 v[164:167], v176 offset:49152
	ds_read_b128 v[186:189], v176 offset:51200
	ds_read_b128 v[190:193], v177 offset:49152
	ds_read_b128 v[194:197], v177 offset:51200
	ds_read_b128 v[198:201], v176 offset:53248
	ds_read_b128 v[202:205], v176 offset:55296
	ds_read_b128 v[206:209], v177 offset:53248
	ds_read_b128 v[210:213], v177 offset:55296
	global_load_lds_dwordx4 v[230:231], off
	v_lshl_add_u64 v[230:231], v[236:237], 0, s[36:37]
	s_mov_b32 m0, s63
	s_nop 0
	global_load_lds_dwordx4 v[230:231], off
	s_barrier
	s_waitcnt lgkmcnt(0)
	s_waitcnt lgkmcnt(0)
	v_mfma_f32_16x16x32_f16 v[62:65], v[130:133], v[164:167], v[62:65]
	v_mfma_f32_16x16x32_f16 v[58:61], v[138:141], v[164:167], v[58:61]
	v_mfma_f32_16x16x32_f16 v[46:49], v[130:133], v[186:189], v[46:49]
	v_mfma_f32_16x16x32_f16 v[42:45], v[138:141], v[186:189], v[42:45]
	v_mfma_f32_16x16x32_f16 v[30:33], v[130:133], v[198:201], v[30:33]
	v_mfma_f32_16x16x32_f16 v[26:29], v[138:141], v[198:201], v[26:29]
	v_mfma_f32_16x16x32_f16 v[14:17], v[130:133], v[202:205], v[14:17]
	v_mfma_f32_16x16x32_f16 v[10:13], v[138:141], v[202:205], v[10:13]
	v_mfma_f32_16x16x32_f16 v[62:65], v[134:137], v[190:193], v[62:65]
	v_mfma_f32_16x16x32_f16 v[58:61], v[142:145], v[190:193], v[58:61]
	v_mfma_f32_16x16x32_f16 v[46:49], v[134:137], v[194:197], v[46:49]
	v_mfma_f32_16x16x32_f16 v[42:45], v[142:145], v[194:197], v[42:45]
	v_mfma_f32_16x16x32_f16 v[30:33], v[134:137], v[206:209], v[30:33]
	v_mfma_f32_16x16x32_f16 v[26:29], v[142:145], v[206:209], v[26:29]
	v_mfma_f32_16x16x32_f16 v[14:17], v[134:137], v[210:213], v[14:17]
	v_mfma_f32_16x16x32_f16 v[10:13], v[142:145], v[210:213], v[10:13]
	s_barrier
	s_add_i32 s50, s50, s54
	v_lshl_add_u64 v[130:131], v[238:239], 0, s[36:37]
	s_mov_b32 m0, s50
	s_nop 0
	global_load_lds_dwordx4 v[130:131], off
	v_lshl_add_u64 v[130:131], v[240:241], 0, s[36:37]
	s_add_i32 m0, s50, 0x2000
	s_nop 0
	global_load_lds_dwordx4 v[130:131], off
	s_waitcnt vmcnt(6)
	s_barrier
	v_mfma_f32_16x16x32_f16 v[54:57], v[214:217], v[164:167], v[54:57]
	v_mfma_f32_16x16x32_f16 v[50:53], v[222:225], v[164:167], v[50:53]
	v_mfma_f32_16x16x32_f16 v[38:41], v[214:217], v[186:189], v[38:41]
	v_mfma_f32_16x16x32_f16 v[34:37], v[222:225], v[186:189], v[34:37]
	v_mfma_f32_16x16x32_f16 v[22:25], v[214:217], v[198:201], v[22:25]
	v_mfma_f32_16x16x32_f16 v[18:21], v[222:225], v[198:201], v[18:21]
	v_mfma_f32_16x16x32_f16 v[6:9], v[214:217], v[202:205], v[6:9]
	v_mfma_f32_16x16x32_f16 v[2:5], v[222:225], v[202:205], v[2:5]
	v_mfma_f32_16x16x32_f16 v[54:57], v[218:221], v[190:193], v[54:57]
	v_mfma_f32_16x16x32_f16 v[50:53], v[226:229], v[190:193], v[50:53]
	v_mfma_f32_16x16x32_f16 v[38:41], v[218:221], v[194:197], v[38:41]
	v_mfma_f32_16x16x32_f16 v[34:37], v[226:229], v[194:197], v[34:37]
	v_mfma_f32_16x16x32_f16 v[22:25], v[218:221], v[206:209], v[22:25]
	v_mfma_f32_16x16x32_f16 v[18:21], v[226:229], v[206:209], v[18:21]
	v_mfma_f32_16x16x32_f16 v[6:9], v[218:221], v[210:213], v[6:9]
	v_mfma_f32_16x16x32_f16 v[2:5], v[226:229], v[210:213], v[2:5]
	s_add_u32 s4, s4, 0x100
	s_addc_u32 s5, s5, 0
	s_add_u32 s75, s75, 0x100
	s_addc_u32 s76, s76, 0
	s_cmp_ge_i32 s77, s64
	s_mov_b32 s50, s77
	s_barrier
	s_cbranch_scc0 .LBB7_21
